# MLA loop: next-tile LDS staging writes moved from the step tail into the P.V section (between its 2nd and 3rd block)
# baseline (speedup 1.0000x reference)
; #define FA_SBAR() __builtin_amdgcn_sched_barrier(0)
; __device__ __forceinline__ void partialSM(f32x16& p0, f32x16& p1, float& m_reg, float& mn, float& alpha, const float C, const float thr) {
;     ...
;   const float mnC = -mn * C;
; #pragma unroll
;   for (int r = 0; r < 16; ++r) p0[r] = fmaf(p0[r], C, mnC);
; #pragma unroll
;   for (int r = 0; r < 16; ++r) p1[r] = fmaf(p1[r], C, mnC);
; #pragma unroll
;   for (int r = 0; r < 16; ++r) p0[r] = __builtin_amdgcn_exp2f(p0[r]);
; }
; __device__ __forceinline__ void finishSM(f32x16& p0, f32x16& p1, float alpha, float& l_reg, bf16x8& pa0, bf16x8& pa1, bf16x8& pa2, bf16x8& pa3) {
; #pragma unroll
;   for (int r = 0; r < 16; ++r) p1[r] = __builtin_amdgcn_exp2f(p1[r]);
;   float ps = 0;
; #pragma unroll
;   for (int r = 0; r < 16; ++r) ps += p0[r];
; #pragma unroll
;   for (int r = 0; r < 16; ++r) ps += p1[r];
;   { auto rr = __builtin_amdgcn_permlane32_swap(__float_as_uint(ps), __float_as_uint(ps), false, false);
;     ps = __uint_as_float(rr[0]) + __uint_as_float(rr[1]); }
;   l_reg = l_reg * alpha + ps;
;   FA_PK4(p0, 0, pa0); FA_PK4(p0, 8, pa1); FA_PK4(p1, 0, pa2); FA_PK4(p1, 8, pa3);
;   s16x4 l0 = tr_read<BASE + v_rd_off(D0, 0, 0)>(vb), h0 = tr_read<BASE + v_rd_off(D0, 0, 1)>(vb), l1 = tr_read<BASE + v_rd_off(D0, 1, 0)>(vb), h1 = tr_read<BASE + v_rd_off(D0, 1, 1)>(vb);
;   s16x4 l2 = tr_read<BASE + v_rd_off(D0, 2, 0)>(vb), h2 = tr_read<BASE + v_rd_off(D0, 2, 1)>(vb), l3 = tr_read<BASE + v_rd_off(D0, 3, 0)>(vb), h3 = tr_read<BASE + v_rd_off(D0, 3, 1)>(vb);
;   asm volatile("s_waitcnt lgkmcnt(0)" : "+v"(l0), "+v"(h0), "+v"(l1), "+v"(h1), "+v"(l2), "+v"(h2), "+v"(l3), "+v"(h3) :: "memory"); FA_SBAR();
.LBB0_1133:
	v_cndmask_b32_e64 v216, v2, v216, s[6:7]
	v_mul_f32_e32 v2, 0xbdd53b94, v216
	v_fmamk_f32 v3, v96, 0x3dd53b94, v2
	v_fmamk_f32 v4, v97, 0x3dd53b94, v2
	v_exp_f32_e32 v3, v3
	v_fmamk_f32 v5, v98, 0x3dd53b94, v2
	v_exp_f32_e32 v4, v4
	v_fmamk_f32 v6, v99, 0x3dd53b94, v2
	v_exp_f32_e32 v5, v5
	v_fmamk_f32 v7, v100, 0x3dd53b94, v2
	v_fmamk_f32 v8, v101, 0x3dd53b94, v2
	v_fmamk_f32 v9, v102, 0x3dd53b94, v2
	v_fmamk_f32 v10, v103, 0x3dd53b94, v2
	v_fmamk_f32 v11, v104, 0x3dd53b94, v2
	v_fmamk_f32 v12, v105, 0x3dd53b94, v2
	v_fmamk_f32 v13, v106, 0x3dd53b94, v2
	v_fmamk_f32 v14, v107, 0x3dd53b94, v2
	v_fmamk_f32 v15, v108, 0x3dd53b94, v2
	v_fmamk_f32 v96, v109, 0x3dd53b94, v2
	v_fmamk_f32 v97, v110, 0x3dd53b94, v2
	v_fmamk_f32 v98, v111, 0x3dd53b94, v2
	v_fmamk_f32 v80, v80, 0x3dd53b94, v2
	v_fmamk_f32 v81, v81, 0x3dd53b94, v2
	v_fmamk_f32 v82, v82, 0x3dd53b94, v2
	v_fmamk_f32 v83, v83, 0x3dd53b94, v2
	v_fmamk_f32 v84, v84, 0x3dd53b94, v2
	v_fmamk_f32 v85, v85, 0x3dd53b94, v2
	v_fmamk_f32 v86, v86, 0x3dd53b94, v2
	v_fmamk_f32 v87, v87, 0x3dd53b94, v2
	v_fmamk_f32 v88, v88, 0x3dd53b94, v2
	v_fmamk_f32 v89, v89, 0x3dd53b94, v2
	v_fmamk_f32 v90, v90, 0x3dd53b94, v2
	v_fmamk_f32 v91, v91, 0x3dd53b94, v2
	v_fmamk_f32 v92, v92, 0x3dd53b94, v2
	v_fmamk_f32 v93, v93, 0x3dd53b94, v2
	v_fmamk_f32 v94, v94, 0x3dd53b94, v2
	v_fmac_f32_e32 v2, 0x3dd53b94, v95
	v_exp_f32_e32 v95, v6
	v_exp_f32_e32 v99, v7
	v_exp_f32_e32 v100, v2
	v_add_f32_e32 v2, 0, v3
	v_exp_f32_e32 v8, v8
	v_add_f32_e32 v2, v4, v2
	v_exp_f32_e32 v9, v9
	v_add_f32_e32 v2, v5, v2
	v_exp_f32_e32 v10, v10
	v_add_f32_e32 v2, v95, v2
	v_exp_f32_e32 v11, v11
	v_add_f32_e32 v2, v99, v2
	v_exp_f32_e32 v12, v12
	v_add_f32_e32 v2, v8, v2
	v_exp_f32_e32 v13, v13
	v_add_f32_e32 v2, v9, v2
	v_exp_f32_e32 v14, v14
	v_add_f32_e32 v2, v10, v2
	v_exp_f32_e32 v15, v15
	v_add_f32_e32 v2, v11, v2
	v_exp_f32_e32 v96, v96
	v_add_f32_e32 v2, v12, v2
	v_exp_f32_e32 v97, v97
	v_add_f32_e32 v2, v13, v2
	v_exp_f32_e32 v98, v98
	v_add_f32_e32 v2, v14, v2
	v_exp_f32_e32 v80, v80
	v_add_f32_e32 v2, v15, v2
	v_exp_f32_e32 v81, v81
	v_add_f32_e32 v2, v96, v2
	v_exp_f32_e32 v82, v82
	v_add_f32_e32 v2, v97, v2
	v_exp_f32_e32 v83, v83
	v_add_f32_e32 v2, v98, v2
	v_exp_f32_e32 v84, v84
	v_add_f32_e32 v2, v80, v2
	v_exp_f32_e32 v85, v85
	v_add_f32_e32 v2, v81, v2
	v_exp_f32_e32 v86, v86
	v_add_f32_e32 v2, v82, v2
	v_exp_f32_e32 v87, v87
	v_add_f32_e32 v2, v83, v2
	v_exp_f32_e32 v88, v88
	v_add_f32_e32 v2, v84, v2
	v_exp_f32_e32 v89, v89
	v_add_f32_e32 v2, v85, v2
	v_exp_f32_e32 v90, v90
	v_add_f32_e32 v2, v86, v2
	v_exp_f32_e32 v91, v91
	v_add_f32_e32 v2, v87, v2
	v_exp_f32_e32 v92, v92
	v_add_f32_e32 v2, v88, v2
	v_exp_f32_e32 v93, v93
	v_add_f32_e32 v2, v89, v2
	v_exp_f32_e32 v94, v94
	v_add_f32_e32 v2, v90, v2
	v_add_f32_e32 v2, v91, v2
	v_add_f32_e32 v2, v92, v2
	v_add_f32_e32 v2, v93, v2
	v_add_f32_e32 v2, v94, v2
	v_add_f32_e32 v6, v100, v2
	v_mov_b32_e32 v7, v6
	s_nop 1
	v_permlane32_swap_b32_e32 v6, v7
	v_cvt_pk_bf16_f32 v2, v3, v4
	v_cvt_pk_bf16_f32 v3, v5, v95
	v_cvt_pk_bf16_f32 v4, v99, v8
	v_cvt_pk_bf16_f32 v5, v9, v10
	v_cvt_pk_bf16_f32 v8, v11, v12
	v_cvt_pk_bf16_f32 v9, v13, v14
	v_cvt_pk_bf16_f32 v10, v15, v96
	v_cvt_pk_bf16_f32 v11, v97, v98
	v_cvt_pk_bf16_f32 v12, v80, v81
	v_cvt_pk_bf16_f32 v13, v82, v83
	v_cvt_pk_bf16_f32 v14, v84, v85
	v_cvt_pk_bf16_f32 v15, v86, v87
	v_cvt_pk_bf16_f32 v80, v88, v89
	v_cvt_pk_bf16_f32 v81, v90, v91
	v_cvt_pk_bf16_f32 v82, v92, v93
	v_cvt_pk_bf16_f32 v83, v94, v100
	s_nop 0
	v_permlane32_swap_b32_e32 v2, v4
	v_permlane32_swap_b32_e32 v3, v5
	v_permlane32_swap_b32_e32 v8, v10
	v_permlane32_swap_b32_e32 v9, v11
	v_permlane32_swap_b32_e32 v12, v14
	v_permlane32_swap_b32_e32 v13, v15
	v_permlane32_swap_b32_e32 v80, v82
	v_permlane32_swap_b32_e32 v81, v83
	v_lshl_add_u32 v100, s51, 14, v213
	ds_read_b64_tr_b16 v[84:85], v100 offset:0
	ds_read_b64_tr_b16 v[86:87], v100 offset:0x800
	ds_read_b64_tr_b16 v[88:89], v100 offset:0x1000
	ds_read_b64_tr_b16 v[90:91], v100 offset:0x1800
	ds_read_b64_tr_b16 v[92:93], v100 offset:0x2000
	ds_read_b64_tr_b16 v[94:95], v100 offset:0x2800
	ds_read_b64_tr_b16 v[96:97], v100 offset:0x3000
	ds_read_b64_tr_b16 v[98:99], v100 offset:0x3800
	s_nop 0
	s_waitcnt lgkmcnt(6)
; #define MLA_SWRITE(bb) do { *(LAS v4u*)(V_lds + (bb) * SHM_V + vst0) = vs0; *(LAS v4u*)(V_lds + (bb) * SHM_V + vst0 + 8192) = vs1; \
;             *(LAS v4u*)(K_lds + (bb) * SHM_K + kst0) = ks0; *(LAS v4u*)(K_lds + (bb) * SHM_K + kst0 + 32 * 384) = ks1; \
;             *(LAS v4u*)(K_lds + (bb) * SHM_K + kst2) = krr; } while (0)
;     ...
;   od = __builtin_amdgcn_mfma_f32_32x32x16_bf16(pa0, FA_PK(l0, h0), od, 0, 0, 0);
;   od = __builtin_amdgcn_mfma_f32_32x32x16_bf16(pa1, FA_PK(l1, h1), od, 0, 0, 0);
;   od = __builtin_amdgcn_mfma_f32_32x32x16_bf16(pa2, FA_PK(l2, h2), od, 0, 0, 0);
;   od = __builtin_amdgcn_mfma_f32_32x32x16_bf16(pa3, FA_PK(l3, h3), od, 0, 0, 0);
; __device__ __forceinline__ void mla_attn_phase(LAS unsigned char* lds, const bf16* Q, const bf16* KV, const bf16* Z, bf16* Oabc, const float* ropec, const float* ropes, int vcu, int G, int tid) {
;     ...
;                     pv_d0(o, vb0 + buf * SHM_V, pa0, pa1, pa2, pa3);
;                 }
;                 if (t + 1 < nt) MLA_SWRITE(buf ^ 1);
	s_nop 0
	v_mfma_f32_32x32x16_bf16 v[64:79], v[2:5], v[84:87], v[64:79]
	ds_read_b64_tr_b16 v[84:85], v100 offset:0x200
	ds_read_b64_tr_b16 v[86:87], v100 offset:0xa00
	s_waitcnt lgkmcnt(6)
	v_mfma_f32_32x32x16_bf16 v[64:79], v[8:11], v[88:91], v[64:79]
	ds_read_b64_tr_b16 v[88:89], v100 offset:0x1200
	ds_read_b64_tr_b16 v[90:91], v100 offset:0x1a00
	s_waitcnt lgkmcnt(6)
	v_mfma_f32_32x32x16_bf16 v[64:79], v[12:15], v[92:95], v[64:79]
	ds_read_b64_tr_b16 v[92:93], v100 offset:0x2200
	ds_read_b64_tr_b16 v[94:95], v100 offset:0x2a00
	s_waitcnt lgkmcnt(6)
	v_mfma_f32_32x32x16_bf16 v[64:79], v[80:83], v[96:99], v[64:79]
	ds_read_b64_tr_b16 v[96:97], v100 offset:0x3200
	ds_read_b64_tr_b16 v[98:99], v100 offset:0x3a00
	s_nop 0
	s_waitcnt lgkmcnt(6)
	s_nop 0
	v_mfma_f32_32x32x16_bf16 v[48:63], v[2:5], v[84:87], v[48:63]
	ds_read_b64_tr_b16 v[84:85], v100 offset:0x400
	ds_read_b64_tr_b16 v[86:87], v100 offset:0xc00
	s_waitcnt lgkmcnt(6)
	v_mfma_f32_32x32x16_bf16 v[48:63], v[8:11], v[88:91], v[48:63]
	ds_read_b64_tr_b16 v[88:89], v100 offset:0x1400
	ds_read_b64_tr_b16 v[90:91], v100 offset:0x1c00
	s_waitcnt lgkmcnt(6)
	v_mfma_f32_32x32x16_bf16 v[48:63], v[12:15], v[92:95], v[48:63]
	ds_read_b64_tr_b16 v[92:93], v100 offset:0x2400
	ds_read_b64_tr_b16 v[94:95], v100 offset:0x2c00
	s_waitcnt lgkmcnt(6)
	v_mfma_f32_32x32x16_bf16 v[48:63], v[80:83], v[96:99], v[48:63]
	ds_read_b64_tr_b16 v[96:97], v100 offset:0x3400
	ds_read_b64_tr_b16 v[98:99], v100 offset:0x3c00
	s_xor_b32 s6, s51, 1
	v_lshl_add_u32 v101, s6, 14, v210
	s_mulk_i32 s6, 0x6000
	s_add_i32 s6, s6, 0
	s_waitcnt vmcnt(3)
	ds_write_b128 v101, v[148:151] offset:49152
	s_waitcnt vmcnt(1)
	ds_write_b128 v101, v[156:159] offset:57344
	v_add_u32_e32 v101, s6, v204
	ds_write_b128 v101, v[144:147]
	ds_write_b128 v101, v[152:155] offset:12288
	v_add_u32_e32 v101, s6, v199
	s_waitcnt vmcnt(0)
	ds_write_b128 v101, v[160:163]
	s_nop 0
	s_waitcnt lgkmcnt(11)
	s_nop 0
	v_mfma_f32_32x32x16_bf16 v[32:47], v[2:5], v[84:87], v[32:47]
	ds_read_b64_tr_b16 v[84:85], v100 offset:0x600
	ds_read_b64_tr_b16 v[86:87], v100 offset:0xe00
	s_waitcnt lgkmcnt(11)
	v_mfma_f32_32x32x16_bf16 v[32:47], v[8:11], v[88:91], v[32:47]
	ds_read_b64_tr_b16 v[88:89], v100 offset:0x1600
	ds_read_b64_tr_b16 v[90:91], v100 offset:0x1e00
	s_waitcnt lgkmcnt(11)
	v_mfma_f32_32x32x16_bf16 v[32:47], v[12:15], v[92:95], v[32:47]
	ds_read_b64_tr_b16 v[92:93], v100 offset:0x2600
	ds_read_b64_tr_b16 v[94:95], v100 offset:0x2e00
	s_waitcnt lgkmcnt(11)
	v_mfma_f32_32x32x16_bf16 v[32:47], v[80:83], v[96:99], v[32:47]
	ds_read_b64_tr_b16 v[96:97], v100 offset:0x3600
	ds_read_b64_tr_b16 v[98:99], v100 offset:0x3e00
	s_nop 0
	s_waitcnt lgkmcnt(6)
	s_nop 0
	v_mfma_f32_32x32x16_bf16 v[16:31], v[2:5], v[84:87], v[16:31]
	s_andn2_b64 vcc, exec, s[14:15]
	s_waitcnt lgkmcnt(4)
	v_mfma_f32_32x32x16_bf16 v[16:31], v[8:11], v[88:91], v[16:31]
	s_waitcnt lgkmcnt(2)
	v_mfma_f32_32x32x16_bf16 v[16:31], v[12:15], v[92:95], v[16:31]
	s_waitcnt lgkmcnt(0)
	v_mfma_f32_32x32x16_bf16 v[16:31], v[80:83], v[96:99], v[16:31]
	s_branch .LBB0_1135
